# speedup vs baseline: 1.0171x; 1.0171x over previous
_Z9ssim_mainPKfS0_S0_Pf:
	v_readfirstlane_b32 s29, v0
	s_load_dwordx4 s[4:7], s[0:1], 0x0
	s_load_dwordx4 s[8:11], s[0:1], 0x10
	s_mov_b32 s51, 0x44800000
	s_mov_b32 s38, 0
	s_mov_b32 s39, -1
	s_lshr_b32 s12, s29, 6
	s_and_b32 s13, s2, 7
	s_lshl_b32 s13, s13, 5
	s_lshr_b32 s14, s2, 3
	s_add_u32 s13, s13, s14
	s_lshr_b32 s14, s13, 3
	s_and_b32 s15, s13, 7
	s_lshl_b32 s16, s14, 20
	s_lshl_b32 s17, s15, 17
	s_add_u32 s16, s16, s17
	s_lshl_b32 s17, s12, 8
	s_add_u32 s16, s16, s17
	s_lshl_b32 s27, s12, 2
	s_add_u32 s27, s27, 0x10000
	v_and_b32_e32 v8, 63, v0
	v_and_b32_e32 v169, 15, v0
	v_bfe_u32 v164, v0, 4, 2
	v_lshrrev_b32_e32 v167, 2, v169
	v_lshlrev_b32_e32 v167, 5, v167
	v_and_b32_e32 v168, 1, v169
	v_lshl_or_b32 v167, v168, 4, v167
	v_bfe_u32 v168, v169, 1, 1
	v_lshl_or_b32 v167, v168, 7, v167
	v_lshl_or_b32 v9, v164, 14, v167
	v_and_b32_e32 v168, 1, v164
	v_lshl_or_b32 v23, v168, 14, v167
	v_lshrrev_b32_e32 v168, 1, v164
	v_lshl_or_b32 v23, v168, 13, v23
	v_add_u32_e32 v237, 0x1000, v9
	v_add_u32_e32 v238, 0x2000, v9
	v_add_u32_e32 v239, 0x3000, v9
	v_add_u32_e32 v240, 0x10000, v9
	v_add_u32_e32 v241, 0x11000, v9
	v_add_u32_e32 v242, 0x12000, v9
	v_add_u32_e32 v243, 0x13000, v9
	s_waitcnt lgkmcnt(0)
	s_load_dwordx8 s[40:47], s[8:9], 0x0
	s_load_dwordx2 s[48:49], s[8:9], 0x20
	s_load_dword s50, s[8:9], 0x28
	s_add_u32 s18, s4, s16
	s_addc_u32 s19, s5, 0
	s_add_u32 s20, s6, s16
	s_addc_u32 s21, s7, 0
	global_load_dwordx4 v[36:39], v9, s[18:19] offset:0 sc1 nt
	global_load_dwordx4 v[40:43], v9, s[18:19] offset:2048 sc1 nt
	global_load_dwordx4 v[68:71], v9, s[20:21] offset:0 sc1 nt
	global_load_dwordx4 v[72:75], v9, s[20:21] offset:2048 sc1 nt
	global_load_dwordx4 v[44:47], v237, s[18:19] offset:0 sc1 nt
	global_load_dwordx4 v[48:51], v237, s[18:19] offset:2048 sc1 nt
	global_load_dwordx4 v[76:79], v237, s[20:21] offset:0 sc1 nt
	global_load_dwordx4 v[80:83], v237, s[20:21] offset:2048 sc1 nt
	global_load_dwordx4 v[52:55], v238, s[18:19] offset:0 sc1 nt
	global_load_dwordx4 v[56:59], v238, s[18:19] offset:2048 sc1 nt
	global_load_dwordx4 v[84:87], v238, s[20:21] offset:0 sc1 nt
	global_load_dwordx4 v[88:91], v238, s[20:21] offset:2048 sc1 nt
	global_load_dwordx4 v[60:63], v239, s[18:19] offset:0 sc1 nt
	global_load_dwordx4 v[64:67], v239, s[18:19] offset:2048 sc1 nt
	global_load_dwordx4 v[92:95], v239, s[20:21] offset:0 sc1 nt
	global_load_dwordx4 v[96:99], v239, s[20:21] offset:2048 sc1 nt
	v_mov_b32_e32 v6, s27
	v_mov_b32_e32 v168, 0
	ds_write_b32 v6, v168 offset:0
	ds_write_b32 v6, v168 offset:32
	ds_write_b32 v6, v168 offset:64
	ds_write_b32 v6, v168 offset:96
	v_lshlrev_b32_e32 v167, 3, v164
	v_xor_b32_e32 v168, 16, v167
	v_sub_u32_e32 v165, v167, v169
	v_sub_u32_e32 v166, v168, v169
	v_add_u32_e32 v172, 0, v165
	v_min_u32_e32 v172, 11, v172
	v_lshlrev_b32_e32 v172, 2, v172
	v_add_u32_e32 v173, 1, v165
	v_min_u32_e32 v173, 11, v173
	v_lshlrev_b32_e32 v173, 2, v173
	v_add_u32_e32 v174, 2, v165
	v_min_u32_e32 v174, 11, v174
	v_lshlrev_b32_e32 v174, 2, v174
	v_add_u32_e32 v175, 3, v165
	v_min_u32_e32 v175, 11, v175
	v_lshlrev_b32_e32 v175, 2, v175
	v_add_u32_e32 v176, 4, v165
	v_min_u32_e32 v176, 11, v176
	v_lshlrev_b32_e32 v176, 2, v176
	v_add_u32_e32 v177, 5, v165
	v_min_u32_e32 v177, 11, v177
	v_lshlrev_b32_e32 v177, 2, v177
	v_add_u32_e32 v178, 6, v165
	v_min_u32_e32 v178, 11, v178
	v_lshlrev_b32_e32 v178, 2, v178
	v_add_u32_e32 v179, 7, v165
	v_min_u32_e32 v179, 11, v179
	v_lshlrev_b32_e32 v179, 2, v179
	v_add_u32_e32 v180, 0, v166
	v_min_u32_e32 v180, 11, v180
	v_lshlrev_b32_e32 v180, 2, v180
	v_add_u32_e32 v181, 1, v166
	v_min_u32_e32 v181, 11, v181
	v_lshlrev_b32_e32 v181, 2, v181
	v_add_u32_e32 v182, 2, v166
	v_min_u32_e32 v182, 11, v182
	v_lshlrev_b32_e32 v182, 2, v182
	v_add_u32_e32 v183, 3, v166
	v_min_u32_e32 v183, 11, v183
	v_lshlrev_b32_e32 v183, 2, v183
	v_add_u32_e32 v184, 4, v166
	v_min_u32_e32 v184, 11, v184
	v_lshlrev_b32_e32 v184, 2, v184
	v_add_u32_e32 v185, 5, v166
	v_min_u32_e32 v185, 11, v185
	v_lshlrev_b32_e32 v185, 2, v185
	v_add_u32_e32 v186, 6, v166
	v_min_u32_e32 v186, 11, v186
	v_lshlrev_b32_e32 v186, 2, v186
	v_add_u32_e32 v187, 7, v166
	v_min_u32_e32 v187, 11, v187
	v_lshlrev_b32_e32 v187, 2, v187
	s_cmp_eq_u32 s15, 7
	s_cselect_b32 s22, 0, 0x20000
	s_add_u32 s84, s18, s22
	s_addc_u32 s85, s19, 0
	s_add_u32 s86, s18, s22
	s_addc_u32 s87, s19, 0
	s_add_u32 s86, s86, 0x1000
	s_addc_u32 s87, s87, 0
	s_add_u32 s88, s20, s22
	s_addc_u32 s89, s21, 0
	s_add_u32 s90, s20, s22
	s_addc_u32 s91, s21, 0
	s_add_u32 s90, s90, 0x1000
	s_addc_u32 s91, s91, 0
	s_waitcnt lgkmcnt(0)
	v_writelane_b32 v171, s40, 0
	v_writelane_b32 v171, s41, 1
	v_writelane_b32 v171, s42, 2
	v_writelane_b32 v171, s43, 3
	v_writelane_b32 v171, s44, 4
	v_writelane_b32 v171, s45, 5
	v_writelane_b32 v171, s46, 6
	v_writelane_b32 v171, s47, 7
	v_writelane_b32 v171, s48, 8
	v_writelane_b32 v171, s49, 9
	v_writelane_b32 v171, s50, 10
	v_writelane_b32 v171, 0, 11
	v_fma_mixlo_f16 v171, v171, s51, 0
	ds_bpermute_b32 v188, v172, v171
	ds_bpermute_b32 v189, v173, v171
	ds_bpermute_b32 v190, v174, v171
	ds_bpermute_b32 v191, v175, v171
	ds_bpermute_b32 v192, v176, v171
	ds_bpermute_b32 v193, v177, v171
	ds_bpermute_b32 v194, v178, v171
	ds_bpermute_b32 v195, v179, v171
	v_mov_b32_e32 v229, 0x44800000
	v_fma_mixlo_f16 v228, s40, v229, 0
	v_cvt_f32_f16_e32 v228, v228
	v_cvt_f64_f32_e32 v[212:213], v228
	v_add_f64 v[212:213], v[212:213], 0
	v_fma_mixlo_f16 v228, s41, v229, 0
	v_cvt_f32_f16_e32 v228, v228
	v_cvt_f64_f32_e32 v[214:215], v228
	v_add_f64 v[212:213], v[212:213], v[214:215]
	v_fma_mixlo_f16 v228, s42, v229, 0
	v_cvt_f32_f16_e32 v228, v228
	v_cvt_f64_f32_e32 v[214:215], v228
	v_add_f64 v[212:213], v[212:213], v[214:215]
	v_fma_mixlo_f16 v228, s43, v229, 0
	v_cvt_f32_f16_e32 v228, v228
	v_cvt_f64_f32_e32 v[214:215], v228
	v_add_f64 v[212:213], v[212:213], v[214:215]
	v_fma_mixlo_f16 v228, s44, v229, 0
	v_cvt_f32_f16_e32 v228, v228
	v_cvt_f64_f32_e32 v[214:215], v228
	v_add_f64 v[212:213], v[212:213], v[214:215]
	v_fma_mixlo_f16 v228, s45, v229, 0
	v_cvt_f32_f16_e32 v228, v228
	v_cvt_f64_f32_e32 v[214:215], v228
	v_add_f64 v[212:213], v[212:213], v[214:215]
	v_fma_mixlo_f16 v228, s46, v229, 0
	v_cvt_f32_f16_e32 v228, v228
	v_cvt_f64_f32_e32 v[214:215], v228
	v_add_f64 v[212:213], v[212:213], v[214:215]
	v_fma_mixlo_f16 v228, s47, v229, 0
	v_cvt_f32_f16_e32 v228, v228
	v_cvt_f64_f32_e32 v[214:215], v228
	v_add_f64 v[212:213], v[212:213], v[214:215]
	v_fma_mixlo_f16 v228, s48, v229, 0
	v_cvt_f32_f16_e32 v228, v228
	v_cvt_f64_f32_e32 v[214:215], v228
	v_add_f64 v[212:213], v[212:213], v[214:215]
	v_fma_mixlo_f16 v228, s49, v229, 0
	v_cvt_f32_f16_e32 v228, v228
	v_cvt_f64_f32_e32 v[214:215], v228
	v_add_f64 v[212:213], v[212:213], v[214:215]
	v_fma_mixlo_f16 v228, s50, v229, 0
	v_cvt_f32_f16_e32 v228, v228
	v_cvt_f64_f32_e32 v[214:215], v228
	v_add_f64 v[212:213], v[212:213], v[214:215]
	s_waitcnt lgkmcnt(7)
	ds_bpermute_b32 v196, v180, v171
	ds_bpermute_b32 v197, v181, v171
	ds_bpermute_b32 v198, v182, v171
	ds_bpermute_b32 v199, v183, v171
	ds_bpermute_b32 v200, v184, v171
	ds_bpermute_b32 v201, v185, v171
	ds_bpermute_b32 v202, v186, v171
	ds_bpermute_b32 v203, v187, v171
	v_mul_f64 v[212:213], v[212:213], v[212:213]
	v_mul_f64 v[216:217], v[212:213], 0.5
	v_add_f64 v[218:219], v[216:217], v[216:217]
	s_mov_b32 s36, 0xeb1c432d
	s_mov_b32 s37, 0x3f1a36e2
	v_mul_f64 v[220:221], v[212:213], s[36:37]
	v_mul_f64 v[222:223], v[216:217], v[218:219]
	v_fmac_f64_e32 v[222:223], v[212:213], v[220:221]
	v_add_f64 v[224:225], v[212:213], v[212:213]
	s_mov_b32 s36, 0x487fcb92
	s_mov_b32 s37, 0x3f4d7dbf
	v_mul_f64 v[226:227], v[212:213], s[36:37]
	v_cvt_f32_f64_e32 v0, v[226:227]
	v_mov_b32_e32 v1, v0
	v_mov_b32_e32 v2, v0
	v_mov_b32_e32 v3, v0
	v_cvt_f32_f64_e32 v10, v[218:219]
	v_cvt_f32_f64_e32 v11, v[222:223]
	v_cvt_f32_f64_e32 v12, v[212:213]
	v_cvt_f32_f64_e32 v13, v[224:225]
	v_mul_f64 v[226:227], v[212:213], v[226:227]
	v_cvt_f32_f64_e32 v14, v[226:227]
	v_lshlrev_b32_e32 v167, 2, v164
	s_cmp_eq_u32 s12, 0
	s_cselect_b32 s23, 6, 64
	v_add_u32_e32 v168, 0, v167
	v_cmp_gt_u32_e32 vcc, s23, v168
	s_nop 1
	v_cndmask_b32_e64 v15, 0, 1.0, vcc
	v_add_u32_e32 v168, 1, v167
	v_cmp_gt_u32_e32 vcc, s23, v168
	s_nop 1
	v_cndmask_b32_e64 v16, 0, 1.0, vcc
	v_add_u32_e32 v168, 2, v167
	v_cmp_gt_u32_e32 vcc, s23, v168
	s_nop 1
	v_cndmask_b32_e64 v17, 0, 1.0, vcc
	v_add_u32_e32 v168, 3, v167
	v_cmp_gt_u32_e32 vcc, s23, v168
	s_nop 1
	v_cndmask_b32_e64 v18, 0, 1.0, vcc
	v_and_b32_e32 v167, 31, v8
	v_lshlrev_b32_e32 v167, 4, v167
	s_lshl_b32 s24, s12, 11
	s_add_i32 s25, s12, 7
	s_and_b32 s25, s25, 7
	s_lshl_b32 s26, s25, 11
	v_or_b32_e32 v4, s24, v167
	v_or_b32_e32 v5, s26, v167
	s_lshl_b32 s28, s25, 2
	s_add_u32 s28, s28, 0x10000
	v_mov_b32_e32 v7, s28
	v_mov_b32_e32 v19, 0
	v_mov_b32_e32 v20, 0
	v_mov_b32_e32 v21, 0
	v_mov_b32_e32 v22, 0
	s_waitcnt lgkmcnt(0)
	v_cmp_lt_u32_e64 s[32:33], 31, v8
	v_cmp_gt_u32_e64 s[34:35], 32, v8
	v_pack_b32_f16 v24, v188, v189
	v_pack_b32_f16 v25, v190, v191
	v_pack_b32_f16 v26, v192, v193
	v_pack_b32_f16 v27, v194, v195
	v_pack_b32_f16 v167, v196, v197
	v_cndmask_b32_e64 v28, 0, v167, s[32:33]
	v_cndmask_b32_e64 v32, 0, v167, s[34:35]
	v_pack_b32_f16 v167, v198, v199
	v_cndmask_b32_e64 v29, 0, v167, s[32:33]
	v_cndmask_b32_e64 v33, 0, v167, s[34:35]
	v_pack_b32_f16 v167, v200, v201
	v_cndmask_b32_e64 v30, 0, v167, s[32:33]
	v_cndmask_b32_e64 v34, 0, v167, s[34:35]
	v_pack_b32_f16 v167, v202, v203
	v_cndmask_b32_e64 v31, 0, v167, s[32:33]
	v_cndmask_b32_e64 v35, 0, v167, s[34:35]
	s_waitcnt lgkmcnt(0)
	s_barrier
	s_cmp_lt_u32 s12, 4
	s_cbranch_scc1 .Lq_noprio
	s_setprio 1
.Lq_noprio:
	s_waitcnt vmcnt(12)
	v_cvt_pk_f16_f32 v164, v36, v40
	v_cvt_pk_f16_f32 v180, v68, v72
	v_pk_add_f16 v164, v164, -0.5 op_sel_hi:[1,0]
	v_pk_add_f16 v180, v180, -0.5 op_sel_hi:[1,0]
	v_pk_mul_f16 v196, v180, v180
	v_pk_mul_f16 v212, v164, v180
	v_pk_fma_f16 v196, v164, v164, v196
	v_cvt_pk_f16_f32 v168, v37, v41
	v_cvt_pk_f16_f32 v184, v69, v73
	v_pk_add_f16 v168, v168, -0.5 op_sel_hi:[1,0]
	v_pk_add_f16 v184, v184, -0.5 op_sel_hi:[1,0]
	v_pk_mul_f16 v200, v184, v184
	v_pk_mul_f16 v216, v168, v184
	v_pk_fma_f16 v200, v168, v168, v200
	v_cvt_pk_f16_f32 v172, v38, v42
	v_cvt_pk_f16_f32 v188, v70, v74
	v_pk_add_f16 v172, v172, -0.5 op_sel_hi:[1,0]
	v_pk_add_f16 v188, v188, -0.5 op_sel_hi:[1,0]
	v_pk_mul_f16 v204, v188, v188
	v_pk_mul_f16 v220, v172, v188
	v_pk_fma_f16 v204, v172, v172, v204
	v_cvt_pk_f16_f32 v176, v39, v43
	v_cvt_pk_f16_f32 v192, v71, v75
	v_pk_add_f16 v176, v176, -0.5 op_sel_hi:[1,0]
	v_pk_add_f16 v192, v192, -0.5 op_sel_hi:[1,0]
	v_pk_mul_f16 v208, v192, v192
	v_pk_mul_f16 v224, v176, v192
	v_pk_fma_f16 v208, v176, v176, v208
	s_waitcnt vmcnt(8)
	v_cvt_pk_f16_f32 v165, v44, v48
	v_cvt_pk_f16_f32 v181, v76, v80
	v_pk_add_f16 v165, v165, -0.5 op_sel_hi:[1,0]
	v_pk_add_f16 v181, v181, -0.5 op_sel_hi:[1,0]
	v_pk_mul_f16 v197, v181, v181
	v_pk_mul_f16 v213, v165, v181
	v_pk_fma_f16 v197, v165, v165, v197
	v_cvt_pk_f16_f32 v169, v45, v49
	v_cvt_pk_f16_f32 v185, v77, v81
	v_pk_add_f16 v169, v169, -0.5 op_sel_hi:[1,0]
	v_pk_add_f16 v185, v185, -0.5 op_sel_hi:[1,0]
	v_pk_mul_f16 v201, v185, v185
	v_pk_mul_f16 v217, v169, v185
	v_pk_fma_f16 v201, v169, v169, v201
	v_cvt_pk_f16_f32 v173, v46, v50
	v_cvt_pk_f16_f32 v189, v78, v82
	v_pk_add_f16 v173, v173, -0.5 op_sel_hi:[1,0]
	v_pk_add_f16 v189, v189, -0.5 op_sel_hi:[1,0]
	v_pk_mul_f16 v205, v189, v189
	v_pk_mul_f16 v221, v173, v189
	v_pk_fma_f16 v205, v173, v173, v205
	v_cvt_pk_f16_f32 v177, v47, v51
	v_cvt_pk_f16_f32 v193, v79, v83
	v_pk_add_f16 v177, v177, -0.5 op_sel_hi:[1,0]
	v_pk_add_f16 v193, v193, -0.5 op_sel_hi:[1,0]
	v_pk_mul_f16 v209, v193, v193
	v_pk_mul_f16 v225, v177, v193
	v_pk_fma_f16 v209, v177, v177, v209
	s_waitcnt vmcnt(4)
	v_cvt_pk_f16_f32 v166, v52, v56
	v_cvt_pk_f16_f32 v182, v84, v88
	v_pk_add_f16 v166, v166, -0.5 op_sel_hi:[1,0]
	v_pk_add_f16 v182, v182, -0.5 op_sel_hi:[1,0]
	v_pk_mul_f16 v198, v182, v182
	v_pk_mul_f16 v214, v166, v182
	v_pk_fma_f16 v198, v166, v166, v198
	v_cvt_pk_f16_f32 v170, v53, v57
	v_cvt_pk_f16_f32 v186, v85, v89
	v_pk_add_f16 v170, v170, -0.5 op_sel_hi:[1,0]
	v_pk_add_f16 v186, v186, -0.5 op_sel_hi:[1,0]
	v_pk_mul_f16 v202, v186, v186
	v_pk_mul_f16 v218, v170, v186
	v_pk_fma_f16 v202, v170, v170, v202
	v_cvt_pk_f16_f32 v174, v54, v58
	v_cvt_pk_f16_f32 v190, v86, v90
	v_pk_add_f16 v174, v174, -0.5 op_sel_hi:[1,0]
	v_pk_add_f16 v190, v190, -0.5 op_sel_hi:[1,0]
	v_pk_mul_f16 v206, v190, v190
	v_pk_mul_f16 v222, v174, v190
	v_pk_fma_f16 v206, v174, v174, v206
	v_cvt_pk_f16_f32 v178, v55, v59
	v_cvt_pk_f16_f32 v194, v87, v91
	v_pk_add_f16 v178, v178, -0.5 op_sel_hi:[1,0]
	v_pk_add_f16 v194, v194, -0.5 op_sel_hi:[1,0]
	v_pk_mul_f16 v210, v194, v194
	v_pk_mul_f16 v226, v178, v194
	v_pk_fma_f16 v210, v178, v178, v210
	s_waitcnt vmcnt(0)
	v_cvt_pk_f16_f32 v167, v60, v64
	v_cvt_pk_f16_f32 v183, v92, v96
	v_pk_add_f16 v167, v167, -0.5 op_sel_hi:[1,0]
	v_pk_add_f16 v183, v183, -0.5 op_sel_hi:[1,0]
	v_pk_mul_f16 v199, v183, v183
	v_pk_mul_f16 v215, v167, v183
	v_pk_fma_f16 v199, v167, v167, v199
	v_cvt_pk_f16_f32 v171, v61, v65
	v_cvt_pk_f16_f32 v187, v93, v97
	v_pk_add_f16 v171, v171, -0.5 op_sel_hi:[1,0]
	v_pk_add_f16 v187, v187, -0.5 op_sel_hi:[1,0]
	v_pk_mul_f16 v203, v187, v187
	v_pk_mul_f16 v219, v171, v187
	v_pk_fma_f16 v203, v171, v171, v203
	v_cvt_pk_f16_f32 v175, v62, v66
	v_cvt_pk_f16_f32 v191, v94, v98
	v_pk_add_f16 v175, v175, -0.5 op_sel_hi:[1,0]
	v_pk_add_f16 v191, v191, -0.5 op_sel_hi:[1,0]
	v_pk_mul_f16 v207, v191, v191
	v_pk_mul_f16 v223, v175, v191
	v_pk_fma_f16 v207, v175, v175, v207
	v_cvt_pk_f16_f32 v179, v63, v67
	v_cvt_pk_f16_f32 v195, v95, v99
	v_pk_add_f16 v179, v179, -0.5 op_sel_hi:[1,0]
	v_pk_add_f16 v195, v195, -0.5 op_sel_hi:[1,0]
	v_pk_mul_f16 v211, v195, v195
	v_pk_mul_f16 v227, v179, v195
	v_pk_fma_f16 v211, v179, v179, v211
	global_load_dwordx4 v[100:103], v240, s[18:19] offset:0 sc1 nt
	global_load_dwordx4 v[104:107], v240, s[18:19] offset:2048 sc1 nt
	global_load_dwordx4 v[132:135], v240, s[20:21] offset:0 sc1 nt
	global_load_dwordx4 v[136:139], v240, s[20:21] offset:2048 sc1 nt
	global_load_dwordx4 v[108:111], v241, s[18:19] offset:0 sc1 nt
	global_load_dwordx4 v[112:115], v241, s[18:19] offset:2048 sc1 nt
	global_load_dwordx4 v[140:143], v241, s[20:21] offset:0 sc1 nt
	global_load_dwordx4 v[144:147], v241, s[20:21] offset:2048 sc1 nt
	global_load_dwordx4 v[116:119], v242, s[18:19] offset:0 sc1 nt
	global_load_dwordx4 v[120:123], v242, s[18:19] offset:2048 sc1 nt
	global_load_dwordx4 v[148:151], v242, s[20:21] offset:0 sc1 nt
	global_load_dwordx4 v[152:155], v242, s[20:21] offset:2048 sc1 nt
	global_load_dwordx4 v[124:127], v243, s[18:19] offset:0 sc1 nt
	global_load_dwordx4 v[128:131], v243, s[18:19] offset:2048 sc1 nt
	global_load_dwordx4 v[156:159], v243, s[20:21] offset:0 sc1 nt
	global_load_dwordx4 v[160:163], v243, s[20:21] offset:2048 sc1 nt
	v_mfma_f32_16x16x32_f16 v[68:71], v[164:167], v[24:27], 0
	v_mfma_f32_16x16x32_f16 v[72:75], v[168:171], v[24:27], 0
	v_mfma_f32_16x16x32_f16 v[76:79], v[172:175], v[24:27], 0
	v_mfma_f32_16x16x32_f16 v[80:83], v[176:179], v[24:27], 0
	v_mfma_f32_16x16x32_f16 v[84:87], v[180:183], v[24:27], 0
	v_mfma_f32_16x16x32_f16 v[88:91], v[184:187], v[24:27], 0
	v_mfma_f32_16x16x32_f16 v[92:95], v[188:191], v[24:27], 0
	v_mfma_f32_16x16x32_f16 v[96:99], v[192:195], v[24:27], 0
	s_nop 1
	v_cvt_pk_f16_f32 v36, v68, v72
	s_nop 0
	v_cvt_pk_f16_f32 v37, v76, v80
	v_cvt_pk_f16_f32 v38, v69, v73
	v_cvt_pk_f16_f32 v39, v77, v81
	v_cvt_pk_f16_f32 v40, v70, v74
	v_cvt_pk_f16_f32 v41, v78, v82
	v_cvt_pk_f16_f32 v42, v71, v75
	v_cvt_pk_f16_f32 v43, v79, v83
	v_mfma_f32_16x16x32_f16 v[68:71], v[196:199], v[24:27], 0
	v_mfma_f32_16x16x32_f16 v[72:75], v[200:203], v[24:27], 0
	v_mfma_f32_16x16x32_f16 v[76:79], v[204:207], v[24:27], 0
	v_mfma_f32_16x16x32_f16 v[80:83], v[208:211], v[24:27], 0
	v_cvt_pk_f16_f32 v44, v84, v88
	v_cvt_pk_f16_f32 v45, v92, v96
	v_cvt_pk_f16_f32 v46, v85, v89
	v_cvt_pk_f16_f32 v47, v93, v97
	v_cvt_pk_f16_f32 v48, v86, v90
	v_cvt_pk_f16_f32 v49, v94, v98
	v_cvt_pk_f16_f32 v50, v87, v91
	v_cvt_pk_f16_f32 v51, v95, v99
	v_mfma_f32_16x16x32_f16 v[84:87], v[212:215], v[24:27], 0
	v_mfma_f32_16x16x32_f16 v[88:91], v[216:219], v[24:27], 0
	v_mfma_f32_16x16x32_f16 v[92:95], v[220:223], v[24:27], 0
	v_mfma_f32_16x16x32_f16 v[96:99], v[224:227], v[24:27], 0
	v_cvt_pk_f16_f32 v52, v68, v72
	v_cvt_pk_f16_f32 v53, v76, v80
	v_cvt_pk_f16_f32 v54, v69, v73
	v_cvt_pk_f16_f32 v55, v77, v81
	v_cvt_pk_f16_f32 v56, v70, v74
	v_cvt_pk_f16_f32 v57, v78, v82
	v_cvt_pk_f16_f32 v58, v71, v75
	v_cvt_pk_f16_f32 v59, v79, v83
	v_cvt_pk_f16_f32 v60, v84, v88
	v_cvt_pk_f16_f32 v61, v92, v96
	v_cvt_pk_f16_f32 v62, v85, v89
	v_cvt_pk_f16_f32 v63, v93, v97
	v_cvt_pk_f16_f32 v64, v86, v90
	v_cvt_pk_f16_f32 v65, v94, v98
	v_cvt_pk_f16_f32 v66, v87, v91
	v_cvt_pk_f16_f32 v67, v95, v99
	s_mov_b64 exec, s[38:39]
	ds_write_b128 v4, v[40:43] offset:0
	ds_write_b128 v4, v[48:51] offset:512
	ds_write_b128 v4, v[56:59] offset:1024
	ds_write_b128 v4, v[64:67] offset:1536
	s_mov_b64 exec, -1
	v_mfma_f32_16x16x32_f16 v[68:71], v[24:27], v[36:39], 0
	v_mfma_f32_16x16x32_f16 v[72:75], v[24:27], v[44:47], 0
	v_mfma_f32_16x16x32_f16 v[76:79], v[24:27], v[52:55], v[0:3]
	v_mfma_f32_16x16x32_f16 v[80:83], v[24:27], v[60:63], 0
	v_mfma_f32_16x16x32_f16 v[84:87], v[28:31], v[36:39], 0
	v_mfma_f32_16x16x32_f16 v[88:91], v[28:31], v[44:47], 0
	v_mfma_f32_16x16x32_f16 v[92:95], v[28:31], v[52:55], v[0:3]
	v_mfma_f32_16x16x32_f16 v[96:99], v[28:31], v[60:63], 0
	v_mfma_f32_16x16x32_f16 v[84:87], v[32:35], v[40:43], v[84:87]
	v_mfma_f32_16x16x32_f16 v[88:91], v[32:35], v[48:51], v[88:91]
	v_mfma_f32_16x16x32_f16 v[92:95], v[32:35], v[56:59], v[92:95]
	v_mfma_f32_16x16x32_f16 v[96:99], v[32:35], v[64:67], v[96:99]
	s_waitcnt lgkmcnt(0)
	ds_write_b32 v6, v6 offset:0
	ds_read_b32 v9, v7 offset:0
	v_mul_f32_e32 v244, v68, v72
	v_mul_f32_e32 v250, v69, v73
	v_mul_f32_e64 v245, -v72, v72
	v_mul_f32_e64 v251, -v73, v73
	v_add_f32_e32 v246, v68, v72
	v_add_f32_e32 v252, v69, v73
	v_fma_f32 v245, -v68, v68, v245
	v_fma_f32 v251, -v69, v69, v251
	v_fma_f32 v247, v10, v246, v11
	v_fma_f32 v253, v10, v252, v11
	v_fma_f32 v246, v13, v80, v14
	v_fma_f32 v252, v13, v81, v14
	v_fma_f32 v248, v12, v76, v245
	v_fma_f32 v254, v12, v77, v251
	v_fma_f32 v249, 2.0, v244, v247
	v_fma_f32 v255, 2.0, v250, v253
	v_sub_f32_e32 v247, v247, v245
	v_sub_f32_e32 v253, v253, v251
	v_fma_f32 v246, -2.0, v244, v246
	v_fma_f32 v252, -2.0, v250, v252
	v_mul_f32_e32 v247, v247, v248
	v_mul_f32_e32 v253, v253, v254
	v_rcp_f32_e32 v247, v247
	v_rcp_f32_e32 v253, v253
	v_mul_f32_e32 v249, v249, v246
	v_mul_f32_e32 v255, v255, v252
	v_fma_f32 v19, v249, v247, v19
	v_fma_f32 v19, v255, v253, v19
	v_mul_f32_e32 v244, v70, v74
	v_mul_f32_e32 v250, v71, v75
	v_mul_f32_e64 v245, -v74, v74
	v_mul_f32_e64 v251, -v75, v75
	v_add_f32_e32 v246, v70, v74
	v_add_f32_e32 v252, v71, v75
	v_fma_f32 v245, -v70, v70, v245
	v_fma_f32 v251, -v71, v71, v251
	v_fma_f32 v247, v10, v246, v11
	v_fma_f32 v253, v10, v252, v11
	v_fma_f32 v246, v13, v82, v14
	v_fma_f32 v252, v13, v83, v14
	v_fma_f32 v248, v12, v78, v245
	v_fma_f32 v254, v12, v79, v251
	v_fma_f32 v249, 2.0, v244, v247
	v_fma_f32 v255, 2.0, v250, v253
	v_sub_f32_e32 v247, v247, v245
	v_sub_f32_e32 v253, v253, v251
	v_fma_f32 v246, -2.0, v244, v246
	v_fma_f32 v252, -2.0, v250, v252
	v_mul_f32_e32 v247, v247, v248
	v_mul_f32_e32 v253, v253, v254
	v_rcp_f32_e32 v247, v247
	v_rcp_f32_e32 v253, v253
	v_mul_f32_e32 v249, v249, v246
	v_mul_f32_e32 v255, v255, v252
	v_fma_f32 v20, v249, v247, v20
	v_fma_f32 v20, v255, v253, v20
	v_mfma_f32_16x16x32_f16 v[68:71], v[24:27], v[40:43], 0
	v_mfma_f32_16x16x32_f16 v[72:75], v[24:27], v[48:51], 0
	v_mfma_f32_16x16x32_f16 v[76:79], v[24:27], v[56:59], v[0:3]
	v_mfma_f32_16x16x32_f16 v[80:83], v[24:27], v[64:67], 0
	s_waitcnt lgkmcnt(0)
	v_cmp_ne_u32_e32 vcc, 0, v9
	s_cbranch_vccnz .Lq_go_0
